# attention tile loops (diff, window, SWA): per-tile LDS address block computed in front of the tile barrier; ring LDS-DMA issue moved from behind the barrier to between the sub-tiles
# speedup vs baseline: 1.0038x; 1.0019x over previous
.LBB0_447:
	s_add_i32 s2, s26, s23
	s_and_b32 s3, s30, 0x18000
	s_add_i32 s3, s3, 0
	s_add_i32 s33, s3, s27
	v_add_u32_e32 v2, s33, v162
	v_add_u32_e32 v4, s33, v164
	v_add_u32_e32 v5, s33, v165
	v_add_u32_e32 v70, s33, v166
	s_ashr_i32 s33, s31, 2
	v_cvt_f32_i32_e32 v170, s33
	v_add_u32_e32 v106, s3, v160
	s_add_i32 s3, s2, 0x7e0
	v_add_u32_e32 v169, 0x4000, v106
	s_cmp_gt_i32 s3, s28
	v_add_u32_e32 v174, v2, v145
	v_add_u32_e32 v173, v4, v145
	v_add_u32_e32 v172, v5, v145
	v_add_u32_e32 v171, v70, v145
	s_barrier
	s_cbranch_scc1 .LBB0_455
	ds_read_b128 v[70:73], v174 offset:4096
	ds_read_b128 v[188:191], v173 offset:4096
	ds_read_b128 v[192:195], v172 offset:4096
	ds_read_b128 v[202:205], v171 offset:4096
	s_and_b32 s3, s3, 0xe0
	v_or_b32_e32 v2, s3, v159
	v_cvt_f32_ubyte0_e32 v2, v2
	v_and_b32_e32 v2, 0x7fff0000, v2
	v_or_b32_sdwa v2, v2, v170 dst_sel:DWORD dst_unused:UNUSED_PAD src0_sel:DWORD src1_sel:WORD_1
	v_cndmask_b32_e64 v2, 0, v2, s[36:37]
	v_mov_b32_e32 v4, v3
	s_waitcnt lgkmcnt(3)
	v_mfma_f32_32x32x16_bf16 v[70:85], v[70:73], v[86:89], 0
	v_mov_b32_e32 v5, v3
	s_add_i32 s3, s2, 0x7ff
	s_cmp_ge_i32 s19, s3
	s_cselect_b64 s[40:41], -1, 0
	s_add_i32 s3, s29, 0xffffffa0
	s_cmp_lt_i32 s3, 0x3fffffe1
	v_add_u32_e32 v175, v169, v150
	s_waitcnt lgkmcnt(2)
	v_mfma_f32_32x32x16_bf16 v[70:85], v[188:191], v[90:93], v[70:85]
	s_cselect_b64 s[42:43], -1, 0
	s_and_b64 s[40:41], s[40:41], s[42:43]
	s_and_b64 vcc, exec, s[40:41]
	s_waitcnt lgkmcnt(1)
	v_mfma_f32_32x32x16_bf16 v[70:85], v[192:195], v[94:97], v[70:85]
	s_waitcnt lgkmcnt(0)
	v_mfma_f32_32x32x16_bf16 v[70:85], v[202:205], v[98:101], v[70:85]
	v_mfma_f32_32x32x16_bf16 v[70:85], v[2:5], v[102:105], v[70:85]
	v_add3_u32 v2, v106, v142, s68
	v_add_u32_e32 v4, v169, v146
	v_add_u32_e32 v5, v169, v148
	ds_read_b64_tr_b16 v[134:135], v2
	ds_read_b64_tr_b16 v[136:137], v2 offset:2048
	ds_read_b64_tr_b16 v[130:131], v4
	ds_read_b64_tr_b16 v[132:133], v4 offset:2048
	ds_read_b64_tr_b16 v[126:127], v5
	ds_read_b64_tr_b16 v[128:129], v5 offset:2048
	ds_read_b64_tr_b16 v[122:123], v175
	ds_read_b64_tr_b16 v[124:125], v175 offset:2048
	ds_read_b64_tr_b16 v[118:119], v2 offset:4096
	ds_read_b64_tr_b16 v[120:121], v2 offset:6144
	ds_read_b64_tr_b16 v[114:115], v4 offset:4096
	ds_read_b64_tr_b16 v[116:117], v4 offset:6144
	ds_read_b64_tr_b16 v[110:111], v5 offset:4096
	ds_read_b64_tr_b16 v[112:113], v5 offset:6144
	ds_read_b64_tr_b16 v[106:107], v175 offset:4096
	ds_read_b64_tr_b16 v[108:109], v175 offset:6144
	s_cbranch_vccnz .LBB0_452
	v_add_u32_e32 v2, s29, v161
	v_add_u32_e32 v4, 0xffffffa0, v2
	v_cmp_gt_u32_e32 vcc, 2.0, v4
	v_add_u32_e32 v4, s23, v163
	v_add_u32_e32 v4, 0x60, v4
	s_nop 2
	v_cndmask_b32_e32 v70, v197, v70, vcc
	v_cmp_lt_u32_e32 vcc, s75, v4
	v_add_u32_e32 v4, 0xffffff9e, v2
	s_nop 0
	v_cndmask_b32_e32 v71, v197, v71, vcc
	v_cmp_gt_u32_e32 vcc, 2.0, v4
	v_add_u32_e32 v4, 0xffffff9d, v2
	s_nop 0
	v_cndmask_b32_e32 v72, v197, v72, vcc
	v_cmp_gt_u32_e32 vcc, 2.0, v4
	v_add_u32_e32 v4, 0xffffff98, v2
	s_nop 0
	v_cndmask_b32_e32 v73, v197, v73, vcc
	v_cmp_gt_u32_e32 vcc, 2.0, v4
	v_add_u32_e32 v4, 0xffffff97, v2
	s_nop 0
	v_cndmask_b32_e32 v74, v197, v74, vcc
	v_cmp_gt_u32_e32 vcc, 2.0, v4
	v_add_u32_e32 v4, 0xffffff96, v2
	s_nop 0
	v_cndmask_b32_e32 v75, v197, v75, vcc
	v_cmp_gt_u32_e32 vcc, 2.0, v4
	v_add_u32_e32 v4, 0xffffff95, v2
	s_nop 0
	v_cndmask_b32_e32 v76, v197, v76, vcc
	v_cmp_gt_u32_e32 vcc, 2.0, v4
	v_add_u32_e32 v4, 0xffffff90, v2
	s_nop 0
	v_cndmask_b32_e32 v77, v197, v77, vcc
	v_cmp_gt_u32_e32 vcc, 2.0, v4
	v_add_u32_e32 v4, 0xffffff8f, v2
	s_nop 0
	v_cndmask_b32_e32 v78, v197, v78, vcc
	v_cmp_gt_u32_e32 vcc, 2.0, v4
	v_add_u32_e32 v4, 0xffffff8e, v2
	s_nop 0
	v_cndmask_b32_e32 v79, v197, v79, vcc
	v_cmp_gt_u32_e32 vcc, 2.0, v4
	v_add_u32_e32 v4, 0xffffff8d, v2
	s_nop 0
	v_cndmask_b32_e32 v80, v197, v80, vcc
	v_cmp_gt_u32_e32 vcc, 2.0, v4
	v_add_u32_e32 v4, 0xffffff88, v2
	s_nop 0
	v_cndmask_b32_e32 v81, v197, v81, vcc
	v_cmp_gt_u32_e32 vcc, 2.0, v4
	v_add_u32_e32 v4, 0xffffff87, v2
	s_nop 0
	v_cndmask_b32_e32 v82, v197, v82, vcc
	v_cmp_gt_u32_e32 vcc, 2.0, v4
	v_add_u32_e32 v4, 0xffffff86, v2
	v_add_u32_e32 v2, 0xffffff85, v2
	v_cndmask_b32_e32 v83, v197, v83, vcc
	v_cmp_gt_u32_e32 vcc, 2.0, v4
	s_nop 1
	v_cndmask_b32_e32 v84, v197, v84, vcc
	v_cmp_gt_u32_e32 vcc, 2.0, v2
	s_nop 1
	v_cndmask_b32_e32 v85, v197, v85, vcc

.LBB0_455:
	s_cmp_ge_u32 s22, s18
	s_cbranch_scc1 .Lring_issue_skip_2
	s_add_i32 s85, s2, 0x700
	s_mul_hi_i32 s86, s85, 0x3600
	s_mulk_i32 s85, 0x3600
	s_add_u32 s88, s14, s85
	s_addc_u32 s89, s15, s86
	s_add_u32 s90, s16, s85
	s_addc_u32 s91, s17, s86
	s_add_i32 s85, s30, 0x18000
	s_and_b32 s85, s85, 0x18000
	s_add_i32 s85, s85, 0
	v_add_u32_e32 v201, s85, v149
	v_mov_b32_e32 v187, v151
	v_readfirstlane_b32 s86, v201
	v_add_u32_e32 v221, s85, v158
	s_mov_b32 m0, s86
	v_add_u32_e32 v221, 0x2000, v221
	global_load_lds_dwordx4 v187, s[88:89]
	v_mov_b32_e32 v187, v153
	v_readfirstlane_b32 s85, v221
	s_mov_b32 m0, s85
	v_add_u32_e32 v221, 0x4000, v201
	global_load_lds_dwordx4 v187, s[88:89]
	v_mov_b32_e32 v187, v155
	v_readfirstlane_b32 s85, v221
	v_add_u32_e32 v201, 0x6000, v201
	s_mov_b32 m0, s85
	v_readfirstlane_b32 s85, v201
	global_load_lds_dwordx4 v187, s[90:91]
	v_mov_b32_e32 v187, v157
	s_mov_b32 m0, s85
	s_nop 0
	global_load_lds_dwordx4 v187, s[90:91]

.Lw_win_4_done:
.LBB0_519:
	s_cmp_eq_u32 s32, 0
	s_cselect_b32 s84, 0, 1
	s_sub_u32 s32, s32, s84
	s_add_i32 s2, s29, s22
	s_add_i32 s3, s27, s21
	s_add_i32 s3, s3, -1
	s_and_b32 s31, s30, 0xc000
	s_add_i32 s33, s31, 0
	s_ashr_i32 s3, s3, 2
	s_add_i32 s31, s2, 0x7e0
	s_cmp_gt_i32 s31, s23
	v_cvt_f32_i32_e32 v111, s3
	s_cselect_b64 s[34:35], -1, 0
	s_add_i32 s3, s2, 0x7ff
	s_cmp_lt_i32 s3, s24
	s_cselect_b64 s[38:39], -1, 0
	v_add_u32_e32 v2, s33, v101
	v_add_u32_e32 v4, s33, v102
	v_add_u32_e32 v5, s33, v103
	v_add_u32_e32 v6, s33, v104
	s_or_b64 s[34:35], s[34:35], s[38:39]
	s_and_b64 vcc, exec, s[34:35]
	v_add_u32_e32 v115, v2, v100
	v_add_u32_e32 v114, v4, v100
	v_add_u32_e32 v113, v5, v100
	v_add_u32_e32 v112, v6, v100
	v_add_u32_e32 v16, s33, v105
	v_add_u32_e32 v17, s33, v106
	s_barrier
	s_cbranch_vccnz .LBB0_527
	ds_read_b128 v[4:7], v115 offset:4096
	ds_read_b128 v[188:191], v114 offset:4096
	ds_read_b128 v[192:195], v113 offset:4096
	ds_read_b128 v[202:205], v112 offset:4096
	s_and_b32 s31, s31, 0xe0
	v_or_b32_e32 v2, s31, v99
	v_cvt_f32_ubyte0_e32 v2, v2
	v_and_b32_e32 v2, 0x7fff0000, v2
	v_or_b32_sdwa v2, v2, v111 dst_sel:DWORD dst_unused:UNUSED_PAD src0_sel:DWORD src1_sel:WORD_1
	v_cndmask_b32_e64 v2, 0, v2, s[36:37]
	s_cmp_ge_i32 s20, s3
	s_cselect_b64 s[34:35], -1, 0
	s_waitcnt lgkmcnt(3)
	v_mfma_f32_32x32x16_bf16 v[50:65], v[4:7], v[74:77], 0
	s_sub_i32 s3, s19, 32
	s_cmpk_lt_i32 s3, 0x1e1
	v_add3_u32 v116, v17, v94, s69
	s_cselect_b64 s[38:39], -1, 0
	s_and_b64 s[34:35], s[34:35], s[38:39]
	s_and_b64 vcc, exec, s[34:35]
	s_waitcnt lgkmcnt(2)
	v_mfma_f32_32x32x16_bf16 v[50:65], v[188:191], v[66:69], v[50:65]
	s_waitcnt lgkmcnt(1)
	v_mfma_f32_32x32x16_bf16 v[50:65], v[192:195], v[70:73], v[50:65]
	s_waitcnt lgkmcnt(0)
	v_mfma_f32_32x32x16_bf16 v[50:65], v[202:205], v[78:81], v[50:65]
	v_mov_b32_e32 v4, v3
	v_mov_b32_e32 v5, v3
	s_nop 1
	v_mfma_f32_32x32x16_bf16 v[50:65], v[2:5], v[82:85], v[50:65]
	v_add3_u32 v2, v16, v94, s69
	ds_read_b64_tr_b16 v[86:87], v2
	ds_read_b64_tr_b16 v[88:89], v2 offset:1024
	ds_read_b64_tr_b16 v[12:13], v116
	ds_read_b64_tr_b16 v[14:15], v116 offset:1024
	ds_read_b64_tr_b16 v[8:9], v2 offset:2048
	ds_read_b64_tr_b16 v[10:11], v2 offset:3072
	ds_read_b64_tr_b16 v[4:5], v116 offset:2048
	ds_read_b64_tr_b16 v[6:7], v116 offset:3072
	s_cbranch_vccnz .LBB0_524
	v_add_u32_e32 v2, s19, v108
	v_subrev_u32_e32 v116, 32, v2
	v_cmp_gt_u32_e32 vcc, s79, v116
	v_add3_u32 v116, v109, s22, 32
	s_nop 5
	v_cndmask_b32_e32 v50, v197, v50, vcc
	v_cmp_lt_u32_e32 vcc, s80, v116
	v_subrev_u32_e32 v116, 34, v2
	s_nop 0
	v_cndmask_b32_e32 v51, v197, v51, vcc
	v_cmp_gt_u32_e32 vcc, s79, v116
	v_subrev_u32_e32 v116, 35, v2
	s_nop 0
	v_cndmask_b32_e32 v52, v197, v52, vcc
	v_cmp_gt_u32_e32 vcc, s79, v116
	v_subrev_u32_e32 v116, 40, v2
	s_nop 0
	v_cndmask_b32_e32 v53, v197, v53, vcc
	v_cmp_gt_u32_e32 vcc, s79, v116
	v_subrev_u32_e32 v116, 41, v2
	s_nop 0
	v_cndmask_b32_e32 v54, v197, v54, vcc
	v_cmp_gt_u32_e32 vcc, s79, v116
	v_subrev_u32_e32 v116, 42, v2
	s_nop 0
	v_cndmask_b32_e32 v55, v197, v55, vcc
	v_cmp_gt_u32_e32 vcc, s79, v116
	v_subrev_u32_e32 v116, 43, v2
	s_nop 0
	v_cndmask_b32_e32 v56, v197, v56, vcc
	v_cmp_gt_u32_e32 vcc, s79, v116
	v_subrev_u32_e32 v116, 48, v2
	s_nop 0
	v_cndmask_b32_e32 v57, v197, v57, vcc
	v_cmp_gt_u32_e32 vcc, s79, v116
	v_subrev_u32_e32 v116, 49, v2
	s_nop 0
	v_cndmask_b32_e32 v58, v197, v58, vcc
	v_cmp_gt_u32_e32 vcc, s79, v116
	v_subrev_u32_e32 v116, 50, v2
	s_nop 0
	v_cndmask_b32_e32 v59, v197, v59, vcc
	v_cmp_gt_u32_e32 vcc, s79, v116
	v_subrev_u32_e32 v116, 51, v2
	s_nop 0
	v_cndmask_b32_e32 v60, v197, v60, vcc
	v_cmp_gt_u32_e32 vcc, s79, v116
	v_subrev_u32_e32 v116, 56, v2
	s_nop 0
	v_cndmask_b32_e32 v61, v197, v61, vcc
	v_cmp_gt_u32_e32 vcc, s79, v116
	v_subrev_u32_e32 v116, 57, v2
	s_nop 0
	v_cndmask_b32_e32 v62, v197, v62, vcc
	v_cmp_gt_u32_e32 vcc, s79, v116
	v_subrev_u32_e32 v116, 58, v2
	v_subrev_u32_e32 v2, 59, v2
	v_cndmask_b32_e32 v63, v197, v63, vcc
	v_cmp_gt_u32_e32 vcc, s79, v116
	s_nop 1
	v_cndmask_b32_e32 v64, v197, v64, vcc
	v_cmp_gt_u32_e32 vcc, s79, v2
	s_nop 1
	v_cndmask_b32_e32 v65, v197, v65, vcc

.LBB0_527:
	s_cmp_gt_i32 s25, s17
	s_cbranch_scc1 .Lring_issue_skip_0
	s_add_i32 s85, s2, 0x700
	s_mul_hi_i32 s86, s85, 0x3600
	s_mulk_i32 s85, 0x3600
	s_add_u32 s88, s12, s85
	s_addc_u32 s89, s13, s86
	s_add_u32 s90, s14, s85
	s_addc_u32 s91, s15, s86
	s_add_i32 s85, s30, 0xc000
	s_and_b32 s85, s85, 0xc000
	v_add_u32_e32 v247, s85, v97
	v_mov_b32_e32 v246, v95
	v_readfirstlane_b32 s85, v247
	v_add_u32_e32 v247, 0x2000, v247
	s_mov_b32 m0, s85
	v_readfirstlane_b32 s85, v247
	global_load_lds_dwordx4 v246, s[88:89]
	v_mov_b32_e32 v246, v96
	s_mov_b32 m0, s85
	s_nop 0
	global_load_lds_dwordx4 v246, s[90:91]

.Lw_swa_4_done:
.LBB0_780:
	s_cmp_eq_u32 s32, 0
	s_cselect_b32 s84, 0, 1
	s_sub_u32 s32, s32, s84
	s_add_i32 s0, s25, s17
	s_add_i32 s1, s23, s18
	s_add_i32 s1, s1, -1
	s_and_b32 s27, s26, 0xc000
	s_add_i32 s34, s27, 0
	s_ashr_i32 s1, s1, 2
	s_add_i32 s27, s0, 0x7e0
	s_cmp_gt_i32 s27, s19
	v_cvt_f32_i32_e32 v114, s1
	s_cselect_b64 s[28:29], -1, 0
	s_add_i32 s1, s0, 0x7ff
	s_cmp_lt_i32 s1, s20
	s_cselect_b64 s[30:31], -1, 0
	v_add_u32_e32 v2, s34, v104
	v_add_u32_e32 v4, s34, v105
	v_add_u32_e32 v5, s34, v106
	v_add_u32_e32 v6, s34, v107
	s_or_b64 s[28:29], s[28:29], s[30:31]
	s_and_b64 vcc, exec, s[28:29]
	v_add_u32_e32 v118, v2, v103
	v_add_u32_e32 v117, v4, v103
	v_add_u32_e32 v116, v5, v103
	v_add_u32_e32 v115, v6, v103
	v_add_u32_e32 v16, s34, v109
	v_add_u32_e32 v17, s34, v110
	s_barrier
	s_cbranch_vccnz .LBB0_788
	ds_read_b128 v[4:7], v118 offset:4096
	ds_read_b128 v[188:191], v117 offset:4096
	ds_read_b128 v[192:195], v116 offset:4096
	ds_read_b128 v[202:205], v115 offset:4096
	s_and_b32 s27, s27, 0xe0
	v_or_b32_e32 v2, s27, v102
	v_cvt_f32_ubyte0_e32 v2, v2
	v_and_b32_e32 v2, 0x7fff0000, v2
	v_or_b32_sdwa v2, v2, v114 dst_sel:DWORD dst_unused:UNUSED_PAD src0_sel:DWORD src1_sel:WORD_1
	v_cndmask_b32_e64 v2, 0, v2, s[36:37]
	s_cmp_ge_i32 s16, s1
	s_cselect_b64 s[28:29], -1, 0
	s_waitcnt lgkmcnt(3)
	v_mfma_f32_32x32x16_bf16 v[50:65], v[4:7], v[66:69], 0
	s_sub_i32 s1, s15, 32
	s_cmpk_lt_i32 s1, 0x61
	v_add3_u32 v119, v17, v96, s69
	s_cselect_b64 s[30:31], -1, 0
	s_and_b64 s[28:29], s[28:29], s[30:31]
	s_and_b64 vcc, exec, s[28:29]
	s_waitcnt lgkmcnt(2)
	v_mfma_f32_32x32x16_bf16 v[50:65], v[188:191], v[70:73], v[50:65]
	s_waitcnt lgkmcnt(1)
	v_mfma_f32_32x32x16_bf16 v[50:65], v[192:195], v[74:77], v[50:65]
	s_waitcnt lgkmcnt(0)
	v_mfma_f32_32x32x16_bf16 v[50:65], v[202:205], v[78:81], v[50:65]
	v_mov_b32_e32 v4, v3
	v_mov_b32_e32 v5, v3
	s_nop 1
	v_mfma_f32_32x32x16_bf16 v[50:65], v[2:5], v[82:85], v[50:65]
	v_add3_u32 v2, v16, v96, s69
	ds_read_b64_tr_b16 v[86:87], v2
	ds_read_b64_tr_b16 v[88:89], v2 offset:1024
	ds_read_b64_tr_b16 v[12:13], v119
	ds_read_b64_tr_b16 v[14:15], v119 offset:1024
	ds_read_b64_tr_b16 v[8:9], v2 offset:2048
	ds_read_b64_tr_b16 v[10:11], v2 offset:3072
	ds_read_b64_tr_b16 v[4:5], v119 offset:2048
	ds_read_b64_tr_b16 v[6:7], v119 offset:3072
	s_cbranch_vccnz .LBB0_785
	v_add_u32_e32 v2, s15, v111
	v_subrev_u32_e32 v119, 32, v2
	v_cmp_gt_u32_e32 vcc, s71, v119
	v_add3_u32 v119, v112, s17, 32
	s_nop 5
	v_cndmask_b32_e32 v50, v197, v50, vcc
	v_cmp_lt_u32_e32 vcc, s47, v119
	v_subrev_u32_e32 v119, 34, v2
	s_nop 0
	v_cndmask_b32_e32 v51, v197, v51, vcc
	v_cmp_gt_u32_e32 vcc, s71, v119
	v_subrev_u32_e32 v119, 35, v2
	s_nop 0
	v_cndmask_b32_e32 v52, v197, v52, vcc
	v_cmp_gt_u32_e32 vcc, s71, v119
	v_subrev_u32_e32 v119, 40, v2
	s_nop 0
	v_cndmask_b32_e32 v53, v197, v53, vcc
	v_cmp_gt_u32_e32 vcc, s71, v119
	v_subrev_u32_e32 v119, 41, v2
	s_nop 0
	v_cndmask_b32_e32 v54, v197, v54, vcc
	v_cmp_gt_u32_e32 vcc, s71, v119
	v_subrev_u32_e32 v119, 42, v2
	s_nop 0
	v_cndmask_b32_e32 v55, v197, v55, vcc
	v_cmp_gt_u32_e32 vcc, s71, v119
	v_subrev_u32_e32 v119, 43, v2
	s_nop 0
	v_cndmask_b32_e32 v56, v197, v56, vcc
	v_cmp_gt_u32_e32 vcc, s71, v119
	v_subrev_u32_e32 v119, 48, v2
	s_nop 0
	v_cndmask_b32_e32 v57, v197, v57, vcc
	v_cmp_gt_u32_e32 vcc, s71, v119
	v_subrev_u32_e32 v119, 49, v2
	s_nop 0
	v_cndmask_b32_e32 v58, v197, v58, vcc
	v_cmp_gt_u32_e32 vcc, s71, v119
	v_subrev_u32_e32 v119, 50, v2
	s_nop 0
	v_cndmask_b32_e32 v59, v197, v59, vcc
	v_cmp_gt_u32_e32 vcc, s71, v119
	v_subrev_u32_e32 v119, 51, v2
	s_nop 0
	v_cndmask_b32_e32 v60, v197, v60, vcc
	v_cmp_gt_u32_e32 vcc, s71, v119
	v_subrev_u32_e32 v119, 56, v2
	s_nop 0
	v_cndmask_b32_e32 v61, v197, v61, vcc
	v_cmp_gt_u32_e32 vcc, s71, v119
	v_subrev_u32_e32 v119, 57, v2
	s_nop 0
	v_cndmask_b32_e32 v62, v197, v62, vcc
	v_cmp_gt_u32_e32 vcc, s71, v119
	v_subrev_u32_e32 v119, 58, v2
	v_subrev_u32_e32 v2, 59, v2
	v_cndmask_b32_e32 v63, v197, v63, vcc
	v_cmp_gt_u32_e32 vcc, s71, v119
	s_nop 1
	v_cndmask_b32_e32 v64, v197, v64, vcc
	v_cmp_gt_u32_e32 vcc, s71, v2
	s_nop 1
	v_cndmask_b32_e32 v65, v197, v65, vcc

.LBB0_788:
	s_cmp_gt_i32 s21, s13
	s_cbranch_scc1 .Lring_issue_skip_1
	s_add_i32 s85, s0, 0x700
	s_mul_hi_i32 s86, s85, 0x3600
	s_mulk_i32 s85, 0x3600
	s_add_u32 s88, s2, s85
	s_addc_u32 s89, s3, s86
	s_add_u32 s90, s10, s85
	s_addc_u32 s91, s11, s86
	s_add_i32 s85, s26, 0xc000
	s_and_b32 s85, s85, 0xc000
	v_add_u32_e32 v247, s85, v99
	v_mov_b32_e32 v246, v97
	v_readfirstlane_b32 s85, v247
	v_add_u32_e32 v247, 0x2000, v247
	s_mov_b32 m0, s85
	v_readfirstlane_b32 s85, v247
	global_load_lds_dwordx4 v246, s[88:89]
	v_mov_b32_e32 v246, v98
	s_mov_b32 m0, s85
	s_nop 0
	global_load_lds_dwordx4 v246, s[90:91]
